# layer-0 LN2 forget-gate logit projection (f32 MFMA): 16 K steps unrolled with a 4-deep operand ring instead of load-wait per step
# baseline (speedup 1.0000x reference)
.LBB0_620:
	s_add_i32 s6, s2, 0
	s_and_b32 s6, s6, 15
	s_lshl_b32 s64, s6, 6
	v_lshl_add_u64 v[100:101], v[20:21], 0, s[64:65]
	v_lshl_add_u64 v[102:103], v[18:19], 0, s[64:65]
	s_lshl_b32 s64, s6, 10
	v_lshl_add_u64 v[104:105], v[22:23], 0, s[64:65]
	global_load_dwordx4 v[26:29], v[100:101], off
	global_load_dwordx4 v[30:33], v[102:103], off
	global_load_dwordx4 v[34:37], v[104:105], off
	s_add_i32 s6, s2, 1
	s_and_b32 s6, s6, 15
	s_lshl_b32 s64, s6, 6
	v_lshl_add_u64 v[100:101], v[20:21], 0, s[64:65]
	v_lshl_add_u64 v[102:103], v[18:19], 0, s[64:65]
	s_lshl_b32 s64, s6, 10
	v_lshl_add_u64 v[104:105], v[22:23], 0, s[64:65]
	global_load_dwordx4 v[38:41], v[100:101], off
	global_load_dwordx4 v[42:45], v[102:103], off
	global_load_dwordx4 v[46:49], v[104:105], off
	s_add_i32 s6, s2, 2
	s_and_b32 s6, s6, 15
	s_lshl_b32 s64, s6, 6
	v_lshl_add_u64 v[100:101], v[20:21], 0, s[64:65]
	v_lshl_add_u64 v[102:103], v[18:19], 0, s[64:65]
	s_lshl_b32 s64, s6, 10
	v_lshl_add_u64 v[104:105], v[22:23], 0, s[64:65]
	global_load_dwordx4 v[50:53], v[100:101], off
	global_load_dwordx4 v[54:57], v[102:103], off
	global_load_dwordx4 v[58:61], v[104:105], off
	s_add_i32 s6, s2, 3
	s_and_b32 s6, s6, 15
	s_lshl_b32 s64, s6, 6
	v_lshl_add_u64 v[100:101], v[20:21], 0, s[64:65]
	v_lshl_add_u64 v[102:103], v[18:19], 0, s[64:65]
	s_lshl_b32 s64, s6, 10
	v_lshl_add_u64 v[104:105], v[22:23], 0, s[64:65]
	global_load_dwordx4 v[88:91], v[100:101], off
	global_load_dwordx4 v[92:95], v[102:103], off
	global_load_dwordx4 v[96:99], v[104:105], off
	s_waitcnt vmcnt(9)
	v_mfma_f32_16x16x4_f32 v[6:9], v30, v34, v[6:9]
	v_mfma_f32_16x16x4_f32 v[2:5], v26, v34, v[2:5]
	v_mfma_f32_16x16x4_f32 v[6:9], v31, v35, v[6:9]
	v_mfma_f32_16x16x4_f32 v[2:5], v27, v35, v[2:5]
	v_mfma_f32_16x16x4_f32 v[6:9], v32, v36, v[6:9]
	v_mfma_f32_16x16x4_f32 v[2:5], v28, v36, v[2:5]
	v_mfma_f32_16x16x4_f32 v[6:9], v33, v37, v[6:9]
	v_mfma_f32_16x16x4_f32 v[2:5], v29, v37, v[2:5]
	s_add_i32 s6, s2, 4
	s_and_b32 s6, s6, 15
	s_lshl_b32 s64, s6, 6
	v_lshl_add_u64 v[100:101], v[20:21], 0, s[64:65]
	v_lshl_add_u64 v[102:103], v[18:19], 0, s[64:65]
	s_lshl_b32 s64, s6, 10
	v_lshl_add_u64 v[104:105], v[22:23], 0, s[64:65]
	global_load_dwordx4 v[26:29], v[100:101], off
	global_load_dwordx4 v[30:33], v[102:103], off
	global_load_dwordx4 v[34:37], v[104:105], off
	s_waitcnt vmcnt(9)
	v_mfma_f32_16x16x4_f32 v[6:9], v42, v46, v[6:9]
	v_mfma_f32_16x16x4_f32 v[2:5], v38, v46, v[2:5]
	v_mfma_f32_16x16x4_f32 v[6:9], v43, v47, v[6:9]
	v_mfma_f32_16x16x4_f32 v[2:5], v39, v47, v[2:5]
	v_mfma_f32_16x16x4_f32 v[6:9], v44, v48, v[6:9]
	v_mfma_f32_16x16x4_f32 v[2:5], v40, v48, v[2:5]
	v_mfma_f32_16x16x4_f32 v[6:9], v45, v49, v[6:9]
	v_mfma_f32_16x16x4_f32 v[2:5], v41, v49, v[2:5]
	s_add_i32 s6, s2, 5
	s_and_b32 s6, s6, 15
	s_lshl_b32 s64, s6, 6
	v_lshl_add_u64 v[100:101], v[20:21], 0, s[64:65]
	v_lshl_add_u64 v[102:103], v[18:19], 0, s[64:65]
	s_lshl_b32 s64, s6, 10
	v_lshl_add_u64 v[104:105], v[22:23], 0, s[64:65]
	global_load_dwordx4 v[38:41], v[100:101], off
	global_load_dwordx4 v[42:45], v[102:103], off
	global_load_dwordx4 v[46:49], v[104:105], off
	s_waitcnt vmcnt(9)
	v_mfma_f32_16x16x4_f32 v[6:9], v54, v58, v[6:9]
	v_mfma_f32_16x16x4_f32 v[2:5], v50, v58, v[2:5]
	v_mfma_f32_16x16x4_f32 v[6:9], v55, v59, v[6:9]
	v_mfma_f32_16x16x4_f32 v[2:5], v51, v59, v[2:5]
	v_mfma_f32_16x16x4_f32 v[6:9], v56, v60, v[6:9]
	v_mfma_f32_16x16x4_f32 v[2:5], v52, v60, v[2:5]
	v_mfma_f32_16x16x4_f32 v[6:9], v57, v61, v[6:9]
	v_mfma_f32_16x16x4_f32 v[2:5], v53, v61, v[2:5]
	s_add_i32 s6, s2, 6
	s_and_b32 s6, s6, 15
	s_lshl_b32 s64, s6, 6
	v_lshl_add_u64 v[100:101], v[20:21], 0, s[64:65]
	v_lshl_add_u64 v[102:103], v[18:19], 0, s[64:65]
	s_lshl_b32 s64, s6, 10
	v_lshl_add_u64 v[104:105], v[22:23], 0, s[64:65]
	global_load_dwordx4 v[50:53], v[100:101], off
	global_load_dwordx4 v[54:57], v[102:103], off
	global_load_dwordx4 v[58:61], v[104:105], off
	s_waitcnt vmcnt(9)
	v_mfma_f32_16x16x4_f32 v[6:9], v92, v96, v[6:9]
	v_mfma_f32_16x16x4_f32 v[2:5], v88, v96, v[2:5]
	v_mfma_f32_16x16x4_f32 v[6:9], v93, v97, v[6:9]
	v_mfma_f32_16x16x4_f32 v[2:5], v89, v97, v[2:5]
	v_mfma_f32_16x16x4_f32 v[6:9], v94, v98, v[6:9]
	v_mfma_f32_16x16x4_f32 v[2:5], v90, v98, v[2:5]
	v_mfma_f32_16x16x4_f32 v[6:9], v95, v99, v[6:9]
	v_mfma_f32_16x16x4_f32 v[2:5], v91, v99, v[2:5]
	s_add_i32 s6, s2, 7
	s_and_b32 s6, s6, 15
	s_lshl_b32 s64, s6, 6
	v_lshl_add_u64 v[100:101], v[20:21], 0, s[64:65]
	v_lshl_add_u64 v[102:103], v[18:19], 0, s[64:65]
	s_lshl_b32 s64, s6, 10
	v_lshl_add_u64 v[104:105], v[22:23], 0, s[64:65]
	global_load_dwordx4 v[88:91], v[100:101], off
	global_load_dwordx4 v[92:95], v[102:103], off
	global_load_dwordx4 v[96:99], v[104:105], off
	s_waitcnt vmcnt(9)
	v_mfma_f32_16x16x4_f32 v[6:9], v30, v34, v[6:9]
	v_mfma_f32_16x16x4_f32 v[2:5], v26, v34, v[2:5]
	v_mfma_f32_16x16x4_f32 v[6:9], v31, v35, v[6:9]
	v_mfma_f32_16x16x4_f32 v[2:5], v27, v35, v[2:5]
	v_mfma_f32_16x16x4_f32 v[6:9], v32, v36, v[6:9]
	v_mfma_f32_16x16x4_f32 v[2:5], v28, v36, v[2:5]
	v_mfma_f32_16x16x4_f32 v[6:9], v33, v37, v[6:9]
	v_mfma_f32_16x16x4_f32 v[2:5], v29, v37, v[2:5]
	s_add_i32 s6, s2, 8
	s_and_b32 s6, s6, 15
	s_lshl_b32 s64, s6, 6
	v_lshl_add_u64 v[100:101], v[20:21], 0, s[64:65]
	v_lshl_add_u64 v[102:103], v[18:19], 0, s[64:65]
	s_lshl_b32 s64, s6, 10
	v_lshl_add_u64 v[104:105], v[22:23], 0, s[64:65]
	global_load_dwordx4 v[26:29], v[100:101], off
	global_load_dwordx4 v[30:33], v[102:103], off
	global_load_dwordx4 v[34:37], v[104:105], off
	s_waitcnt vmcnt(9)
	v_mfma_f32_16x16x4_f32 v[6:9], v42, v46, v[6:9]
	v_mfma_f32_16x16x4_f32 v[2:5], v38, v46, v[2:5]
	v_mfma_f32_16x16x4_f32 v[6:9], v43, v47, v[6:9]
	v_mfma_f32_16x16x4_f32 v[2:5], v39, v47, v[2:5]
	v_mfma_f32_16x16x4_f32 v[6:9], v44, v48, v[6:9]
	v_mfma_f32_16x16x4_f32 v[2:5], v40, v48, v[2:5]
	v_mfma_f32_16x16x4_f32 v[6:9], v45, v49, v[6:9]
	v_mfma_f32_16x16x4_f32 v[2:5], v41, v49, v[2:5]
	s_add_i32 s6, s2, 9
	s_and_b32 s6, s6, 15
	s_lshl_b32 s64, s6, 6
	v_lshl_add_u64 v[100:101], v[20:21], 0, s[64:65]
	v_lshl_add_u64 v[102:103], v[18:19], 0, s[64:65]
	s_lshl_b32 s64, s6, 10
	v_lshl_add_u64 v[104:105], v[22:23], 0, s[64:65]
	global_load_dwordx4 v[38:41], v[100:101], off
	global_load_dwordx4 v[42:45], v[102:103], off
	global_load_dwordx4 v[46:49], v[104:105], off
	s_waitcnt vmcnt(9)
	v_mfma_f32_16x16x4_f32 v[6:9], v54, v58, v[6:9]
	v_mfma_f32_16x16x4_f32 v[2:5], v50, v58, v[2:5]
	v_mfma_f32_16x16x4_f32 v[6:9], v55, v59, v[6:9]
	v_mfma_f32_16x16x4_f32 v[2:5], v51, v59, v[2:5]
	v_mfma_f32_16x16x4_f32 v[6:9], v56, v60, v[6:9]
	v_mfma_f32_16x16x4_f32 v[2:5], v52, v60, v[2:5]
	v_mfma_f32_16x16x4_f32 v[6:9], v57, v61, v[6:9]
	v_mfma_f32_16x16x4_f32 v[2:5], v53, v61, v[2:5]
	s_add_i32 s6, s2, 10
	s_and_b32 s6, s6, 15
	s_lshl_b32 s64, s6, 6
	v_lshl_add_u64 v[100:101], v[20:21], 0, s[64:65]
	v_lshl_add_u64 v[102:103], v[18:19], 0, s[64:65]
	s_lshl_b32 s64, s6, 10
	v_lshl_add_u64 v[104:105], v[22:23], 0, s[64:65]
	global_load_dwordx4 v[50:53], v[100:101], off
	global_load_dwordx4 v[54:57], v[102:103], off
	global_load_dwordx4 v[58:61], v[104:105], off
	s_waitcnt vmcnt(9)
	v_mfma_f32_16x16x4_f32 v[6:9], v92, v96, v[6:9]
	v_mfma_f32_16x16x4_f32 v[2:5], v88, v96, v[2:5]
	v_mfma_f32_16x16x4_f32 v[6:9], v93, v97, v[6:9]
	v_mfma_f32_16x16x4_f32 v[2:5], v89, v97, v[2:5]
	v_mfma_f32_16x16x4_f32 v[6:9], v94, v98, v[6:9]
	v_mfma_f32_16x16x4_f32 v[2:5], v90, v98, v[2:5]
	v_mfma_f32_16x16x4_f32 v[6:9], v95, v99, v[6:9]
	v_mfma_f32_16x16x4_f32 v[2:5], v91, v99, v[2:5]
	s_add_i32 s6, s2, 11
	s_and_b32 s6, s6, 15
	s_lshl_b32 s64, s6, 6
	v_lshl_add_u64 v[100:101], v[20:21], 0, s[64:65]
	v_lshl_add_u64 v[102:103], v[18:19], 0, s[64:65]
	s_lshl_b32 s64, s6, 10
	v_lshl_add_u64 v[104:105], v[22:23], 0, s[64:65]
	global_load_dwordx4 v[88:91], v[100:101], off
	global_load_dwordx4 v[92:95], v[102:103], off
	global_load_dwordx4 v[96:99], v[104:105], off
	s_waitcnt vmcnt(9)
	v_mfma_f32_16x16x4_f32 v[6:9], v30, v34, v[6:9]
	v_mfma_f32_16x16x4_f32 v[2:5], v26, v34, v[2:5]
	v_mfma_f32_16x16x4_f32 v[6:9], v31, v35, v[6:9]
	v_mfma_f32_16x16x4_f32 v[2:5], v27, v35, v[2:5]
	v_mfma_f32_16x16x4_f32 v[6:9], v32, v36, v[6:9]
	v_mfma_f32_16x16x4_f32 v[2:5], v28, v36, v[2:5]
	v_mfma_f32_16x16x4_f32 v[6:9], v33, v37, v[6:9]
	v_mfma_f32_16x16x4_f32 v[2:5], v29, v37, v[2:5]
	s_add_i32 s6, s2, 12
	s_and_b32 s6, s6, 15
	s_lshl_b32 s64, s6, 6
	v_lshl_add_u64 v[100:101], v[20:21], 0, s[64:65]
	v_lshl_add_u64 v[102:103], v[18:19], 0, s[64:65]
	s_lshl_b32 s64, s6, 10
	v_lshl_add_u64 v[104:105], v[22:23], 0, s[64:65]
	global_load_dwordx4 v[26:29], v[100:101], off
	global_load_dwordx4 v[30:33], v[102:103], off
	global_load_dwordx4 v[34:37], v[104:105], off
	s_waitcnt vmcnt(9)
	v_mfma_f32_16x16x4_f32 v[6:9], v42, v46, v[6:9]
	v_mfma_f32_16x16x4_f32 v[2:5], v38, v46, v[2:5]
	v_mfma_f32_16x16x4_f32 v[6:9], v43, v47, v[6:9]
	v_mfma_f32_16x16x4_f32 v[2:5], v39, v47, v[2:5]
	v_mfma_f32_16x16x4_f32 v[6:9], v44, v48, v[6:9]
	v_mfma_f32_16x16x4_f32 v[2:5], v40, v48, v[2:5]
	v_mfma_f32_16x16x4_f32 v[6:9], v45, v49, v[6:9]
	v_mfma_f32_16x16x4_f32 v[2:5], v41, v49, v[2:5]
	s_add_i32 s6, s2, 13
	s_and_b32 s6, s6, 15
	s_lshl_b32 s64, s6, 6
	v_lshl_add_u64 v[100:101], v[20:21], 0, s[64:65]
	v_lshl_add_u64 v[102:103], v[18:19], 0, s[64:65]
	s_lshl_b32 s64, s6, 10
	v_lshl_add_u64 v[104:105], v[22:23], 0, s[64:65]
	global_load_dwordx4 v[38:41], v[100:101], off
	global_load_dwordx4 v[42:45], v[102:103], off
	global_load_dwordx4 v[46:49], v[104:105], off
	s_waitcnt vmcnt(9)
	v_mfma_f32_16x16x4_f32 v[6:9], v54, v58, v[6:9]
	v_mfma_f32_16x16x4_f32 v[2:5], v50, v58, v[2:5]
	v_mfma_f32_16x16x4_f32 v[6:9], v55, v59, v[6:9]
	v_mfma_f32_16x16x4_f32 v[2:5], v51, v59, v[2:5]
	v_mfma_f32_16x16x4_f32 v[6:9], v56, v60, v[6:9]
	v_mfma_f32_16x16x4_f32 v[2:5], v52, v60, v[2:5]
	v_mfma_f32_16x16x4_f32 v[6:9], v57, v61, v[6:9]
	v_mfma_f32_16x16x4_f32 v[2:5], v53, v61, v[2:5]
	s_add_i32 s6, s2, 14
	s_and_b32 s6, s6, 15
	s_lshl_b32 s64, s6, 6
	v_lshl_add_u64 v[100:101], v[20:21], 0, s[64:65]
	v_lshl_add_u64 v[102:103], v[18:19], 0, s[64:65]
	s_lshl_b32 s64, s6, 10
	v_lshl_add_u64 v[104:105], v[22:23], 0, s[64:65]
	global_load_dwordx4 v[50:53], v[100:101], off
	global_load_dwordx4 v[54:57], v[102:103], off
	global_load_dwordx4 v[58:61], v[104:105], off
	s_waitcnt vmcnt(9)
	v_mfma_f32_16x16x4_f32 v[6:9], v92, v96, v[6:9]
	v_mfma_f32_16x16x4_f32 v[2:5], v88, v96, v[2:5]
	v_mfma_f32_16x16x4_f32 v[6:9], v93, v97, v[6:9]
	v_mfma_f32_16x16x4_f32 v[2:5], v89, v97, v[2:5]
	v_mfma_f32_16x16x4_f32 v[6:9], v94, v98, v[6:9]
	v_mfma_f32_16x16x4_f32 v[2:5], v90, v98, v[2:5]
	v_mfma_f32_16x16x4_f32 v[6:9], v95, v99, v[6:9]
	v_mfma_f32_16x16x4_f32 v[2:5], v91, v99, v[2:5]
	s_add_i32 s6, s2, 15
	s_and_b32 s6, s6, 15
	s_lshl_b32 s64, s6, 6
	v_lshl_add_u64 v[100:101], v[20:21], 0, s[64:65]
	v_lshl_add_u64 v[102:103], v[18:19], 0, s[64:65]
	s_lshl_b32 s64, s6, 10
	v_lshl_add_u64 v[104:105], v[22:23], 0, s[64:65]
	global_load_dwordx4 v[88:91], v[100:101], off
	global_load_dwordx4 v[92:95], v[102:103], off
	global_load_dwordx4 v[96:99], v[104:105], off
	s_waitcnt vmcnt(9)
	v_mfma_f32_16x16x4_f32 v[6:9], v30, v34, v[6:9]
	v_mfma_f32_16x16x4_f32 v[2:5], v26, v34, v[2:5]
	v_mfma_f32_16x16x4_f32 v[6:9], v31, v35, v[6:9]
	v_mfma_f32_16x16x4_f32 v[2:5], v27, v35, v[2:5]
	v_mfma_f32_16x16x4_f32 v[6:9], v32, v36, v[6:9]
	v_mfma_f32_16x16x4_f32 v[2:5], v28, v36, v[2:5]
	v_mfma_f32_16x16x4_f32 v[6:9], v33, v37, v[6:9]
	v_mfma_f32_16x16x4_f32 v[2:5], v29, v37, v[2:5]
	s_waitcnt vmcnt(6)
	v_mfma_f32_16x16x4_f32 v[6:9], v42, v46, v[6:9]
	v_mfma_f32_16x16x4_f32 v[2:5], v38, v46, v[2:5]
	v_mfma_f32_16x16x4_f32 v[6:9], v43, v47, v[6:9]
	v_mfma_f32_16x16x4_f32 v[2:5], v39, v47, v[2:5]
	v_mfma_f32_16x16x4_f32 v[6:9], v44, v48, v[6:9]
	v_mfma_f32_16x16x4_f32 v[2:5], v40, v48, v[2:5]
	v_mfma_f32_16x16x4_f32 v[6:9], v45, v49, v[6:9]
	v_mfma_f32_16x16x4_f32 v[2:5], v41, v49, v[2:5]
	s_waitcnt vmcnt(3)
	v_mfma_f32_16x16x4_f32 v[6:9], v54, v58, v[6:9]
	v_mfma_f32_16x16x4_f32 v[2:5], v50, v58, v[2:5]
	v_mfma_f32_16x16x4_f32 v[6:9], v55, v59, v[6:9]
	v_mfma_f32_16x16x4_f32 v[2:5], v51, v59, v[2:5]
	v_mfma_f32_16x16x4_f32 v[6:9], v56, v60, v[6:9]
	v_mfma_f32_16x16x4_f32 v[2:5], v52, v60, v[2:5]
	v_mfma_f32_16x16x4_f32 v[6:9], v57, v61, v[6:9]
	v_mfma_f32_16x16x4_f32 v[2:5], v53, v61, v[2:5]
	s_waitcnt vmcnt(0)
	v_mfma_f32_16x16x4_f32 v[6:9], v92, v96, v[6:9]
	v_mfma_f32_16x16x4_f32 v[2:5], v88, v96, v[2:5]
	v_mfma_f32_16x16x4_f32 v[6:9], v93, v97, v[6:9]
	v_mfma_f32_16x16x4_f32 v[2:5], v89, v97, v[2:5]
	v_mfma_f32_16x16x4_f32 v[6:9], v94, v98, v[6:9]
	v_mfma_f32_16x16x4_f32 v[2:5], v90, v98, v[2:5]
	v_mfma_f32_16x16x4_f32 v[6:9], v95, v99, v[6:9]
	v_mfma_f32_16x16x4_f32 v[2:5], v91, v99, v[2:5]


	s_setprio 0
	s_nop 6
	ds_write2_b32 v25, v6, v7 offset1:48
	ds_write2_b32 v25, v8, v9 offset0:96 offset1:144
	v_add_u32_e32 v6, 0xc00, v25
	ds_write2_b32 v6, v2, v3 offset1:48
	ds_write2_b32 v6, v4, v5 offset0:96 offset1:144
	s_waitcnt lgkmcnt(0)
	s_barrier
	s_and_saveexec_b64 s[6:7], s[0:1]
	s_cbranch_execz .LBB0_624
	s_mov_b64 s[10:11], 0
	v_mov_b32_e32 v2, v11
	v_mov_b32_e32 v3, v70
